# baseline (speedup 1.0000x reference)
.LBB1_4:
	v_mfma_f32_32x32x16_f16 v[66:81], v[66:69], v[144:147], 0
	v_add_u32_e32 v181, s31, v215
	ds_read_b64_tr_b16 v[172:173], v181 offset:49152
	ds_read_b64_tr_b16 v[174:175], v181 offset:49664
	v_add_f32_e32 v86, v50, v51
	v_add_f32_e32 v86, v52, v86
	v_add_f32_e32 v86, v53, v86
	v_add_f32_e32 v86, v54, v86
	v_add_f32_e32 v86, v55, v86
	s_waitcnt lgkmcnt(9)
	v_cvt_pk_f16_f32 v128, v50, v51
	v_cvt_pk_f16_f32 v129, v52, v53
	s_nop 0
	ds_read_b64_tr_b16 v[176:177], v181 offset:53248
	ds_read_b64_tr_b16 v[178:179], v181 offset:53760
	v_add_f32_e32 v50, v56, v86
	s_waitcnt lgkmcnt(10)
	v_mfma_f32_32x32x16_f16 v[82:97], v[82:85], v[144:147], 0
	v_add_f32_e32 v50, v57, v50
	v_add_f32_e32 v50, v58, v50
	v_add_f32_e32 v50, v59, v50
	v_cvt_pk_f16_f32 v130, v54, v55
	v_cvt_pk_f16_f32 v131, v56, v57
	s_nop 0
	ds_read_b64_tr_b16 v[122:123], v181 offset:50176
	ds_read_b64_tr_b16 v[124:125], v181 offset:50688
	s_waitcnt lgkmcnt(11)
	v_mfma_f32_32x32x16_f16 v[66:81], v[168:171], v[140:143], v[66:81]
	v_add_f32_e32 v50, v60, v50
	v_add_f32_e32 v50, v61, v50
	v_add_f32_e32 v50, v62, v50
	v_add_f32_e32 v50, v63, v50
	v_cvt_pk_f16_f32 v106, v58, v59
	v_cvt_pk_f16_f32 v107, v60, v61
	s_nop 0
	ds_read_b64_tr_b16 v[118:119], v181 offset:54272
	ds_read_b64_tr_b16 v[120:121], v181 offset:54784
	s_waitcnt lgkmcnt(12)
	v_mfma_f32_32x32x16_f16 v[82:97], v[164:167], v[140:143], v[82:97]
	v_add_f32_e32 v50, v64, v50
	v_add_f32_e32 v50, v65, v50
	v_add_f32_e32 v50, v34, v50
	v_add_f32_e32 v50, v35, v50
	v_cvt_pk_f16_f32 v108, v62, v63
	v_cvt_pk_f16_f32 v109, v64, v65
	s_nop 0
	ds_read_b64_tr_b16 v[114:115], v181 offset:51200
	ds_read_b64_tr_b16 v[116:117], v181 offset:51712
	s_waitcnt lgkmcnt(13)
	v_mfma_f32_32x32x16_f16 v[66:81], v[160:163], v[136:139], v[66:81]
	v_add_f32_e32 v50, v36, v50
	v_add_f32_e32 v50, v37, v50
	v_add_f32_e32 v50, v38, v50
	v_add_f32_e32 v50, v39, v50
	v_cvt_pk_f16_f32 v102, v34, v35
	v_cvt_pk_f16_f32 v103, v36, v37
	s_nop 0
	ds_read_b64_tr_b16 v[110:111], v181 offset:55296
	ds_read_b64_tr_b16 v[112:113], v181 offset:55808
	s_waitcnt lgkmcnt(14)
	v_mfma_f32_32x32x16_f16 v[82:97], v[156:159], v[136:139], v[82:97]
	v_add_f32_e32 v34, v40, v50
	v_add_f32_e32 v34, v41, v34
	v_add_f32_e32 v34, v42, v34
	v_add_f32_e32 v34, v43, v34
	v_cvt_pk_f16_f32 v104, v38, v39
	v_cvt_pk_f16_f32 v105, v40, v41
	s_nop 0
	ds_read_b64_tr_b16 v[156:157], v181 offset:52224
	ds_read_b64_tr_b16 v[158:159], v181 offset:52736
	s_waitcnt lgkmcnt(14)
	v_mfma_f32_32x32x16_f16 v[66:81], v[152:155], v[132:135], v[66:81]
	v_add_f32_e32 v34, v44, v34
	v_add_f32_e32 v34, v45, v34
	v_add_f32_e32 v34, v46, v34
	v_add_f32_e32 v34, v47, v34
	v_cvt_pk_f16_f32 v98, v42, v43
	v_cvt_pk_f16_f32 v99, v44, v45
	s_nop 0
	ds_read_b64_tr_b16 v[152:153], v181 offset:56320
	ds_read_b64_tr_b16 v[154:155], v181 offset:56832
	v_mfma_f32_32x32x16_f16 v[82:97], v[148:151], v[132:135], v[82:97]
	v_add_f32_e32 v34, v48, v34
	v_add_f32_e32 v34, v49, v34
	v_add_f32_e32 v160, 0, v34
	v_cvt_pk_f16_f32 v100, v46, v47
	v_cvt_pk_f16_f32 v101, v48, v49
	s_nop 0
	s_add_i32 s49, s33, s46
	s_sub_i32 s3, s49, 17
	s_add_i32 s2, s46, -1
	s_min_i32 s3, s3, s33
	s_cmp_gt_u32 s2, s44
	s_cselect_b32 s2, s3, s2
	s_ashr_i32 s3, s2, 31
	s_lshl_b64 s[2:3], s[2:3], 18
	v_lshl_add_u64 v[34:35], v[194:195], 0, s[2:3]
	s_add_i32 s2, s48, s41
	s_mov_b32 s3, m0
	s_mov_b32 m0, s2
	s_nop 0
	global_load_lds_dwordx4 v[34:35], off
	s_mov_b32 m0, s3
	v_lshl_add_u64 v[34:35], v[34:35], 0, s[22:23]
	s_addk_i32 s2, 0x2000
	s_mov_b32 s3, m0
	s_mov_b32 m0, s2
	s_nop 0
	global_load_lds_dwordx4 v[34:35], off
	s_mov_b32 m0, s3
	s_add_i32 s2, s45, s40
	s_mov_b32 s3, m0
	s_mov_b32 m0, s2
	s_nop 0
	global_load_lds_dwordx4 v[126:127], off
	s_mov_b32 m0, s3
	v_lshl_add_u64 v[34:35], v[126:127], 0, s[22:23]
	s_addk_i32 s2, 0x2000
	s_mov_b32 s3, m0
	s_mov_b32 m0, s2
	s_nop 0
	global_load_lds_dwordx4 v[34:35], off
	s_mov_b32 m0, s3
	s_and_b64 vcc, exec, s[20:21]
	s_mov_b64 s[2:3], -1
	s_cbranch_vccz .LBB1_20
	s_andn2_b64 vcc, exec, s[2:3]
	s_cbranch_vccnz .LBB1_8

.LBB1_11:
	v_mfma_f32_32x32x16_f16 v[50:65], v[50:53], v[144:147], 0
	s_add_i32 s2, s45, 0x4000
	s_cmpk_lg_u32 s45, 0x8000
	s_cselect_b32 s43, s2, 0
	v_add_u32_e32 v156, s48, v215
	ds_read_b64_tr_b16 v[118:119], v156 offset:49152
	ds_read_b64_tr_b16 v[120:121], v156 offset:49664
	v_add_f32_e32 v38, v66, v67
	v_add_f32_e32 v38, v68, v38
	v_add_f32_e32 v38, v69, v38
	v_add_f32_e32 v38, v70, v38
	v_add_f32_e32 v38, v71, v38
	s_waitcnt lgkmcnt(9)
	v_cvt_pk_f16_f32 v128, v66, v67
	v_cvt_pk_f16_f32 v129, v68, v69
	s_nop 0
	ds_read_b64_tr_b16 v[152:153], v156 offset:53248
	ds_read_b64_tr_b16 v[154:155], v156 offset:53760
	v_add_f32_e32 v66, v72, v38
	s_waitcnt lgkmcnt(10)
	v_mfma_f32_32x32x16_f16 v[34:49], v[34:37], v[144:147], 0
	v_add_f32_e32 v66, v73, v66
	v_add_f32_e32 v66, v74, v66
	v_add_f32_e32 v66, v75, v66
	v_cvt_pk_f16_f32 v130, v70, v71
	v_cvt_pk_f16_f32 v131, v72, v73
	s_nop 0
	ds_read_b64_tr_b16 v[148:149], v156 offset:50176
	ds_read_b64_tr_b16 v[150:151], v156 offset:50688
	s_waitcnt lgkmcnt(11)
	v_mfma_f32_32x32x16_f16 v[50:65], v[122:125], v[140:143], v[50:65]
	v_add_f32_e32 v66, v76, v66
	v_add_f32_e32 v66, v77, v66
	v_add_f32_e32 v66, v78, v66
	v_add_f32_e32 v66, v79, v66
	v_cvt_pk_f16_f32 v106, v74, v75
	v_cvt_pk_f16_f32 v107, v76, v77
	s_nop 0
	ds_read_b64_tr_b16 v[122:123], v156 offset:54272
	ds_read_b64_tr_b16 v[124:125], v156 offset:54784
	s_waitcnt lgkmcnt(12)
	v_mfma_f32_32x32x16_f16 v[34:49], v[172:175], v[140:143], v[34:49]
	v_add_f32_e32 v66, v80, v66
	v_add_f32_e32 v66, v81, v66
	v_add_f32_e32 v66, v82, v66
	v_add_f32_e32 v66, v83, v66
	v_cvt_pk_f16_f32 v108, v78, v79
	v_cvt_pk_f16_f32 v109, v80, v81
	s_nop 0
	ds_read_b64_tr_b16 v[114:115], v156 offset:51200
	ds_read_b64_tr_b16 v[116:117], v156 offset:51712
	s_waitcnt lgkmcnt(13)
	v_mfma_f32_32x32x16_f16 v[50:65], v[176:179], v[136:139], v[50:65]
	v_add_f32_e32 v66, v84, v66
	v_add_f32_e32 v66, v85, v66
	v_add_f32_e32 v66, v86, v66
	v_add_f32_e32 v66, v87, v66
	v_cvt_pk_f16_f32 v102, v82, v83
	v_cvt_pk_f16_f32 v103, v84, v85
	s_nop 0
	ds_read_b64_tr_b16 v[110:111], v156 offset:55296
	ds_read_b64_tr_b16 v[112:113], v156 offset:55808
	s_waitcnt lgkmcnt(14)
	v_mfma_f32_32x32x16_f16 v[34:49], v[164:167], v[136:139], v[34:49]
	v_add_f32_e32 v82, v88, v66
	v_add_f32_e32 v82, v89, v82
	v_add_f32_e32 v82, v90, v82
	v_add_f32_e32 v82, v91, v82
	v_cvt_pk_f16_f32 v104, v86, v87
	v_cvt_pk_f16_f32 v105, v88, v89
	s_nop 0
	ds_read_b64_tr_b16 v[172:173], v156 offset:52224
	ds_read_b64_tr_b16 v[174:175], v156 offset:52736
	s_waitcnt lgkmcnt(14)
	v_mfma_f32_32x32x16_f16 v[50:65], v[168:171], v[132:135], v[50:65]
	v_add_f32_e32 v82, v92, v82
	v_add_f32_e32 v82, v93, v82
	v_add_f32_e32 v82, v94, v82
	v_add_f32_e32 v82, v95, v82
	v_cvt_pk_f16_f32 v98, v90, v91
	v_cvt_pk_f16_f32 v99, v92, v93
	s_nop 0
	ds_read_b64_tr_b16 v[176:177], v156 offset:56320
	ds_read_b64_tr_b16 v[178:179], v156 offset:56832
	v_mfma_f32_32x32x16_f16 v[34:49], v[160:163], v[132:135], v[34:49]
	v_add_f32_e32 v82, v96, v82
	v_add_f32_e32 v82, v97, v82
	v_add_f32_e32 v156, 0, v82
	v_cvt_pk_f16_f32 v100, v94, v95
	v_cvt_pk_f16_f32 v101, v96, v97
	s_nop 0
	s_add_i32 s49, s49, -16
	s_min_i32 s50, s49, s33
	s_cmp_gt_u32 s46, s44
	s_cselect_b64 s[2:3], -1, 0
	s_and_b64 s[48:49], s[2:3], exec
	s_cselect_b32 s48, s50, s46
	s_ashr_i32 s49, s48, 31
	s_lshl_b64 s[48:49], s[48:49], 18
	v_lshl_add_u64 v[82:83], v[194:195], 0, s[48:49]
	s_add_i32 s48, s45, s41
	s_mov_b32 s49, m0
	s_mov_b32 m0, s48
	s_nop 0
	global_load_lds_dwordx4 v[82:83], off
	s_mov_b32 m0, s49
	v_lshl_add_u64 v[82:83], v[82:83], 0, s[22:23]
	s_addk_i32 s48, 0x2000
	s_mov_b32 s49, m0
	s_mov_b32 m0, s48
	s_nop 0
	global_load_lds_dwordx4 v[82:83], off
	s_mov_b32 m0, s49
	v_lshl_add_u64 v[82:83], v[126:127], 0, s[24:25]
	s_add_i32 s48, s43, s40
	s_mov_b32 s49, m0
	s_mov_b32 m0, s48
	s_nop 0
	global_load_lds_dwordx4 v[82:83], off
	s_mov_b32 m0, s49
	v_lshl_add_u64 v[82:83], v[126:127], 0, s[26:27]
	s_addk_i32 s48, 0x2000
	s_mov_b32 s49, m0
	s_mov_b32 m0, s48
	s_nop 0
	global_load_lds_dwordx4 v[82:83], off
	s_mov_b32 m0, s49
	s_andn2_b64 vcc, exec, s[30:31]
	s_mov_b64 s[30:31], -1
	s_cbranch_vccz .LBB1_24
	s_andn2_b64 vcc, exec, s[30:31]
	s_cbranch_vccnz .LBB1_15
